# v23 + grid-barrier leader no longer waits for the cross-XCD release add to be acknowledged before releasing its own XCD
# speedup vs baseline: 1.0044x; 1.0044x over previous
.LBB0_118:
	s_or_b64 exec, exec, s[28:29]
	s_mov_b64 s[28:29], exec
	v_mbcnt_lo_u32_b32 v1, s28, 0
	v_mbcnt_hi_u32_b32 v1, s29, v1
	v_cmp_eq_u32_e32 vcc, 0, v1
	s_and_saveexec_b64 s[38:39], vcc
	s_cbranch_execz .LBB0_120
	s_bcnt1_i32_b64 s4, s[28:29]
	v_mov_b32_e32 v1, s4
	v_readlane_b32 s4, v254, 45
	v_readlane_b32 s5, v254, 46
	s_nop 4
	global_atomic_add v115, v1, s[4:5]

.LBB0_269:
	s_or_b64 exec, exec, s[26:27]
	s_mov_b64 s[26:27], exec
	v_mbcnt_lo_u32_b32 v1, s26, 0
	v_mbcnt_hi_u32_b32 v1, s27, v1
	v_cmp_eq_u32_e32 vcc, 0, v1
	s_and_saveexec_b64 s[28:29], vcc
	s_cbranch_execz .LBB0_271
	s_bcnt1_i32_b64 s4, s[26:27]
	v_mov_b32_e32 v1, s4
	v_readlane_b32 s4, v254, 45
	v_readlane_b32 s5, v254, 46
	s_nop 4
	global_atomic_add v115, v1, s[4:5]

.LBB0_444:
	s_or_b64 exec, exec, s[10:11]
	s_mov_b64 s[10:11], exec
	v_mbcnt_lo_u32_b32 v1, s10, 0
	v_mbcnt_hi_u32_b32 v1, s11, v1
	v_cmp_eq_u32_e32 vcc, 0, v1
	s_and_saveexec_b64 s[26:27], vcc
	s_cbranch_execz .LBB0_446
	s_bcnt1_i32_b64 s4, s[10:11]
	v_mov_b32_e32 v1, s4
	v_readlane_b32 s4, v254, 45
	v_readlane_b32 s5, v254, 46
	s_nop 4
	global_atomic_add v115, v1, s[4:5]

.LBB0_600:
	s_or_b64 exec, exec, s[10:11]
	s_mov_b64 s[10:11], exec
	v_mbcnt_lo_u32_b32 v1, s10, 0
	v_mbcnt_hi_u32_b32 v1, s11, v1
	v_cmp_eq_u32_e32 vcc, 0, v1
	s_and_saveexec_b64 s[28:29], vcc
	s_cbranch_execz .LBB0_602
	s_bcnt1_i32_b64 s4, s[10:11]
	v_mov_b32_e32 v1, s4
	v_readlane_b32 s4, v254, 45
	v_readlane_b32 s5, v254, 46
	s_nop 4
	global_atomic_add v115, v1, s[4:5]

.LBB0_1052:
	s_or_b64 exec, exec, s[4:5]
	s_mov_b64 s[4:5], exec
	v_mbcnt_lo_u32_b32 v1, s4, 0
	v_mbcnt_hi_u32_b32 v1, s5, v1
	v_cmp_eq_u32_e32 vcc, 0, v1
	s_and_saveexec_b64 s[8:9], vcc
	s_cbranch_execz .LBB0_1054
	s_bcnt1_i32_b64 s4, s[4:5]
	v_mov_b32_e32 v1, s4
	v_readlane_b32 s4, v254, 45
	v_readlane_b32 s5, v254, 46
	s_nop 4
	global_atomic_add v115, v1, s[4:5]

.LBB0_1155:
	s_or_b64 exec, exec, s[8:9]
	s_mov_b64 s[8:9], exec
	v_mbcnt_lo_u32_b32 v1, s8, 0
	v_mbcnt_hi_u32_b32 v1, s9, v1
	v_cmp_eq_u32_e32 vcc, 0, v1
	s_and_saveexec_b64 s[10:11], vcc
	s_cbranch_execz .LBB0_1157
	s_bcnt1_i32_b64 s7, s[8:9]
	v_readlane_b32 s8, v254, 45
	v_mov_b32_e32 v1, s7
	v_readlane_b32 s9, v254, 46
	s_nop 4
	global_atomic_add v115, v1, s[8:9]
